# speedup vs baseline: 1.0165x; 1.0112x over previous
.Lmy_ptbl:
	global_load_dword v9, v[4:5], off
	v_lshl_add_u64 v[12:13], v[4:5], 0, s[18:19]
	v_cmp_gt_u32_e64 s[4:5], 34, v7
	v_mov_b32_e32 v11, 0
	s_and_saveexec_b64 s[16:17], s[4:5]
	global_load_dword v11, v[12:13], off
	s_mov_b64 exec, s[16:17]
	v_add_u32_e32 v10, 64, v7
	v_cmp_gt_u32_e32 vcc, s3, v7
	s_waitcnt vmcnt(0)
	v_add_u32_e32 v2, v9, v11
	v_cndmask_b32_e32 v9, 0, v9, vcc
	v_cmp_gt_u32_e32 vcc, s3, v10
	s_nop 1
	v_cndmask_b32_e32 v11, 0, v11, vcc
	v_add_u32_e32 v3, v9, v11
	s_or_b64 exec, exec, s[16:17]
	v_mbcnt_lo_u32_b32 v4, -1, 0
	v_mbcnt_hi_u32_b32 v4, -1, v4
	v_and_b32_e32 v5, 64, v4
	v_add_u32_e32 v5, 64, v5
	v_xor_b32_e32 v8, 32, v4
	v_cmp_lt_i32_e32 vcc, v8, v5
	v_xor_b32_e32 v10, 16, v4
	v_xor_b32_e32 v11, 8, v4
	v_cndmask_b32_e32 v8, v4, v8, vcc
	v_lshlrev_b32_e32 v8, 2, v8
	ds_bpermute_b32 v9, v8, v3
	v_cmp_lt_i32_e32 vcc, v10, v5
	ds_bpermute_b32 v8, v8, v2
	v_xor_b32_e32 v12, 4, v4
	s_waitcnt lgkmcnt(0)
	v_add_u32_e32 v3, v9, v3
	v_cndmask_b32_e32 v9, v4, v10, vcc
	v_lshlrev_b32_e32 v9, 2, v9
	ds_bpermute_b32 v10, v9, v3
	v_cmp_lt_i32_e32 vcc, v11, v5
	v_add_u32_e32 v2, v8, v2
	ds_bpermute_b32 v8, v9, v2
	v_xor_b32_e32 v9, 2, v4
	s_waitcnt lgkmcnt(1)
	v_add_u32_e32 v3, v10, v3
	v_cndmask_b32_e32 v10, v4, v11, vcc
	v_lshlrev_b32_e32 v10, 2, v10
	ds_bpermute_b32 v11, v10, v3
	s_waitcnt lgkmcnt(1)
	v_add_u32_e32 v2, v8, v2
	v_cmp_lt_i32_e32 vcc, v12, v5
	ds_bpermute_b32 v8, v10, v2
	s_waitcnt lgkmcnt(1)
	v_add_u32_e32 v3, v11, v3
	v_cndmask_b32_e32 v11, v4, v12, vcc
	v_lshlrev_b32_e32 v11, 2, v11
	ds_bpermute_b32 v12, v11, v3
	s_waitcnt lgkmcnt(1)
	v_add_u32_e32 v2, v8, v2
	v_cmp_lt_i32_e32 vcc, v9, v5
	ds_bpermute_b32 v8, v11, v2
	s_waitcnt lgkmcnt(1)
	v_add_u32_e32 v3, v12, v3
	v_cndmask_b32_e32 v9, v4, v9, vcc
	v_lshlrev_b32_e32 v9, 2, v9
	ds_bpermute_b32 v10, v9, v3
	s_waitcnt lgkmcnt(1)
	v_add_u32_e32 v2, v8, v2
	ds_bpermute_b32 v8, v9, v2
	s_waitcnt lgkmcnt(1)
	v_add_u32_e32 v3, v10, v3
	v_xor_b32_e32 v10, 1, v4
	v_cmp_lt_i32_e32 vcc, v10, v5
	s_waitcnt lgkmcnt(0)
	v_add_u32_e32 v2, v8, v2
	v_cndmask_b32_e32 v4, v4, v10, vcc
	v_lshlrev_b32_e32 v4, 2, v4
	ds_bpermute_b32 v5, v4, v3
	ds_bpermute_b32 v4, v4, v2
	v_cmp_eq_u32_e32 vcc, 0, v7
	s_and_b64 exec, exec, vcc
	s_cbranch_execz .LBB1_10
	s_waitcnt lgkmcnt(1)
	v_add_u32_e32 v3, v5, v3
	v_mov_b32_e32 v5, 0x24040
	v_lshl_or_b32 v5, v6, 2, v5
	s_cmp_lg_u32 s3, 0
	ds_write_b32 v5, v3
	s_cbranch_scc1 .LBB1_10
	s_waitcnt lgkmcnt(1)
	v_add_u32_e32 v2, v4, v2
	global_store_dword v1, v2, s[14:15]
